# baseline (speedup 1.0000x reference)
.LBB1_4:
	s_load_dwordx2 s[12:13], s[0:1], 0x10
	s_cmpk_lt_u32 s2, 0x200
	s_cselect_b64 s[10:11], -1, 0
	v_readfirstlane_b32 s25, v0
	s_and_b64 vcc, exec, s[10:11]
	s_cbranch_vccnz .LBB1_6
	s_setprio 2

.LBB1_12:
	s_andn2_b64 vcc, exec, s[16:17]
	s_cbranch_vccnz .LBB1_14
	s_setprio 3
.LBB1_14:
	ds_read_b64_tr_b16 v[66:67], v108 offset:2560
	ds_read_b64_tr_b16 v[64:65], v108
	ds_read_b64_tr_b16 v[68:69], v108 offset:32
	ds_read_b64_tr_b16 v[110:111], v108 offset:64
	ds_read_b64_tr_b16 v[114:115], v108 offset:96
	ds_read_b64_tr_b16 v[70:71], v108 offset:2592
	ds_read_b64_tr_b16 v[112:113], v108 offset:2624
	ds_read_b64_tr_b16 v[116:117], v108 offset:2656
	s_waitcnt vmcnt(3) lgkmcnt(6)
	v_mfma_f32_16x16x32_f16 v[60:63], v[64:67], v[92:95], v[60:63]
	s_mov_b64 s[16:17], -1
	s_and_b64 vcc, exec, s[10:11]
	v_mfma_f32_16x16x32_f16 v[56:59], v[64:67], v[80:83], v[56:59]
	v_mfma_f32_16x16x32_f16 v[52:55], v[64:67], v[88:91], v[52:55]
	s_waitcnt vmcnt(2)
	v_mfma_f32_16x16x32_f16 v[48:51], v[64:67], v[84:87], v[48:51]
	s_waitcnt lgkmcnt(2)
	v_mfma_f32_16x16x32_f16 v[44:47], v[68:71], v[92:95], v[44:47]
	v_mfma_f32_16x16x32_f16 v[40:43], v[68:71], v[80:83], v[40:43]
	v_mfma_f32_16x16x32_f16 v[36:39], v[68:71], v[88:91], v[36:39]
	v_mfma_f32_16x16x32_f16 v[32:35], v[68:71], v[84:87], v[32:35]
	s_waitcnt lgkmcnt(1)
	v_mfma_f32_16x16x32_f16 v[28:31], v[110:113], v[92:95], v[28:31]
	v_mfma_f32_16x16x32_f16 v[24:27], v[110:113], v[80:83], v[24:27]
	v_mfma_f32_16x16x32_f16 v[20:23], v[110:113], v[88:91], v[20:23]
	v_mfma_f32_16x16x32_f16 v[16:19], v[110:113], v[84:87], v[16:19]
	s_waitcnt lgkmcnt(0)
	v_mfma_f32_16x16x32_f16 v[12:15], v[114:117], v[92:95], v[12:15]
	v_mfma_f32_16x16x32_f16 v[8:11], v[114:117], v[80:83], v[8:11]
	v_mfma_f32_16x16x32_f16 v[4:7], v[114:117], v[88:91], v[4:7]
	v_mfma_f32_16x16x32_f16 v[0:3], v[114:117], v[84:87], v[0:3]
	s_cbranch_vccz .LBB1_16
	s_setprio 0
	s_mov_b64 s[16:17], 0
.LBB1_16:
	s_andn2_b64 vcc, exec, s[16:17]
	s_cbranch_vccnz .LBB1_18
	s_setprio 2
.LBB1_18:
	s_and_saveexec_b64 s[44:45], s[8:9]
	global_load_dwordx4 v[84:87], v[102:103], off offset:-3072
	global_load_dwordx4 v[88:91], v[102:103], off offset:-2048
	global_load_dwordx4 v[92:95], v[102:103], off offset:-1024
	global_load_dwordx4 v[80:83], v[102:103], off
	s_mov_b64 exec, s[44:45]
	s_add_i32 s27, s26, 2
	s_cmp_gt_u32 s26, 17
	s_cselect_b64 s[16:17], -1, 0
	s_cmp_lt_u32 s26, 18
	s_cselect_b64 s[18:19], -1, 0
	s_and_b64 s[20:21], s[18:19], exec
	s_cselect_b32 s4, s27, s26
	s_lshl_b32 s4, s4, 11
	s_lshl_b64 s[20:21], s[4:5], 2
	v_lshl_add_u64 v[64:65], v[96:97], 0, s[20:21]
	v_lshl_add_u64 v[66:67], v[98:99], 0, s[20:21]
	s_and_saveexec_b64 s[44:45], s[18:19]
	global_load_dwordx4 v[68:71], v[64:65], off nt
	s_and_b64 exec, exec, s[0:1]
	global_load_dwordx4 v[64:67], v[66:67], off nt
	s_mov_b64 exec, s[44:45]
	s_waitcnt vmcnt(7)
	v_pk_fma_f32 v[104:105], v[76:77], v[76:77], v[104:105]
	v_pk_fma_f32 v[106:107], v[78:79], v[78:79], v[106:107]
	v_cvt_pk_f16_f32 v79, v78, v79
	v_cvt_pk_f16_f32 v78, v76, v77
	ds_write_b64 v109, v[78:79] offset:5120
	s_and_saveexec_b64 s[20:21], s[0:1]
	s_cbranch_execz .LBB1_20
	s_waitcnt vmcnt(6)
	v_pk_fma_f32 v[104:105], v[72:73], v[72:73], v[104:105]
	v_pk_fma_f32 v[106:107], v[74:75], v[74:75], v[106:107]
	v_cvt_pk_f16_f32 v75, v74, v75
	v_cvt_pk_f16_f32 v74, v72, v73
	ds_write_b64 v109, v[74:75] offset:8320

.LBB1_23:
	s_andn2_b64 vcc, exec, s[2:3]
	s_cbranch_vccnz .LBB1_25
	s_setprio 3
.LBB1_25:
	s_waitcnt vmcnt(6)
	ds_read_b64_tr_b16 v[74:75], v108 offset:7680
	ds_read_b64_tr_b16 v[72:73], v108 offset:5120
	ds_read_b64_tr_b16 v[76:77], v108 offset:5152
	ds_read_b64_tr_b16 v[110:111], v108 offset:5184
	ds_read_b64_tr_b16 v[114:115], v108 offset:5216
	ds_read_b64_tr_b16 v[78:79], v108 offset:7712
	ds_read_b64_tr_b16 v[112:113], v108 offset:7744
	ds_read_b64_tr_b16 v[116:117], v108 offset:7776
	s_waitcnt vmcnt(5) lgkmcnt(6)
	v_mfma_f32_16x16x32_f16 v[60:63], v[72:75], v[84:87], v[60:63]
	s_mov_b64 s[2:3], -1
	s_and_b64 vcc, exec, s[10:11]
	s_waitcnt vmcnt(4)
	v_mfma_f32_16x16x32_f16 v[56:59], v[72:75], v[88:91], v[56:59]
	s_waitcnt vmcnt(3)
	v_mfma_f32_16x16x32_f16 v[52:55], v[72:75], v[92:95], v[52:55]
	s_waitcnt vmcnt(2)
	v_mfma_f32_16x16x32_f16 v[48:51], v[72:75], v[80:83], v[48:51]
	s_waitcnt lgkmcnt(2)
	v_mfma_f32_16x16x32_f16 v[44:47], v[76:79], v[84:87], v[44:47]
	v_mfma_f32_16x16x32_f16 v[40:43], v[76:79], v[88:91], v[40:43]
	v_mfma_f32_16x16x32_f16 v[36:39], v[76:79], v[92:95], v[36:39]
	v_mfma_f32_16x16x32_f16 v[32:35], v[76:79], v[80:83], v[32:35]
	s_waitcnt lgkmcnt(1)
	v_mfma_f32_16x16x32_f16 v[28:31], v[110:113], v[84:87], v[28:31]
	v_mfma_f32_16x16x32_f16 v[24:27], v[110:113], v[88:91], v[24:27]
	v_mfma_f32_16x16x32_f16 v[20:23], v[110:113], v[92:95], v[20:23]
	v_mfma_f32_16x16x32_f16 v[16:19], v[110:113], v[80:83], v[16:19]
	s_waitcnt lgkmcnt(0)
	v_mfma_f32_16x16x32_f16 v[12:15], v[114:117], v[84:87], v[12:15]
	v_mfma_f32_16x16x32_f16 v[8:11], v[114:117], v[88:91], v[8:11]
	v_mfma_f32_16x16x32_f16 v[4:7], v[114:117], v[92:95], v[4:7]
	v_mfma_f32_16x16x32_f16 v[0:3], v[114:117], v[80:83], v[0:3]
	s_cbranch_vccz .LBB1_27
	s_setprio 0
	s_mov_b64 s[2:3], 0
.LBB1_27:
	s_andn2_b64 vcc, exec, s[2:3]
	s_cbranch_vccnz .LBB1_29
	s_setprio 2
